# baseline (speedup 1.0000x reference)
.LBB1_31:
	s_waitcnt vmcnt(6)
	v_mbcnt_lo_u32_b32 v64, -1, 0
	v_mbcnt_hi_u32_b32 v100, -1, v64
	s_andn2_b32 s25, s25, 63
	v_add_u32_e32 v64, s25, v100
	v_ashrrev_i32_e32 v64, 4, v64
	s_movk_i32 s0, 0x44
	v_and_b32_e32 v101, 15, v100
	v_mul_lo_u32 v64, v64, s0
	v_lshl_add_u32 v64, v101, 2, v64
	s_and_b64 vcc, exec, s[8:9]
	s_barrier
	ds_write_b32 v64, v104
	ds_write_b32 v64, v105 offset:1360
	ds_write_b32 v64, v106 offset:2720
	ds_write_b32 v64, v107 offset:4080
	s_waitcnt lgkmcnt(0)
	s_barrier
	s_cbranch_vccz .LBB1_38
	v_and_b32_e32 v64, 3, v100
	v_and_b32_e32 v65, 0x7c, v100
	s_movk_i32 s0, 0x550
	v_mad_u32_u24 v70, v64, s0, v65
	ds_read2_b32 v[64:65], v70 offset1:17
	ds_read2_b32 v[66:67], v70 offset0:34 offset1:51
	ds_read2_b32 v[68:69], v70 offset0:68 offset1:85
	s_mov_b32 s0, 0xf800000
	s_lshl_b32 s10, s23, 8
	s_waitcnt lgkmcnt(2)
	v_add_f32_e32 v64, 0, v64
	v_add_f32_e32 v64, v64, v65
	s_waitcnt lgkmcnt(1)
	v_add_f32_e32 v66, v64, v66
	ds_read2_b32 v[64:65], v70 offset0:102 offset1:119
	v_add_f32_e32 v66, v66, v67
	s_waitcnt lgkmcnt(1)
	v_add_f32_e32 v66, v66, v68
	v_add_f32_e32 v68, v66, v69
	ds_read2_b32 v[66:67], v70 offset0:136 offset1:153
	s_waitcnt lgkmcnt(1)
	v_add_f32_e32 v64, v68, v64
	ds_read2_b32 v[68:69], v70 offset0:170 offset1:187
	v_add_f32_e32 v71, v64, v65
	ds_read2_b32 v[64:65], v70 offset0:204 offset1:221
	s_waitcnt lgkmcnt(2)
	v_add_f32_e32 v66, v71, v66
	v_add_f32_e32 v66, v66, v67
	s_waitcnt lgkmcnt(1)
	v_add_f32_e32 v66, v66, v68
	v_add_f32_e32 v66, v66, v69
	s_waitcnt lgkmcnt(0)
	v_add_f32_e32 v64, v66, v64
	ds_read2_b32 v[66:67], v70 offset0:238 offset1:255
	v_add_u32_e32 v70, 0x400, v70
	ds_read2_b32 v[68:69], v70 offset0:16 offset1:33
	v_add_f32_e32 v71, v64, v65
	ds_read2_b32 v[64:65], v70 offset0:50 offset1:67
	s_waitcnt lgkmcnt(2)
	v_add_f32_e32 v66, v71, v66
	v_add_f32_e32 v66, v66, v67
	s_waitcnt lgkmcnt(1)
	v_add_f32_e32 v66, v66, v68
	v_add_f32_e32 v66, v66, v69
	s_waitcnt lgkmcnt(0)
	v_add_f32_e32 v64, v66, v64
	v_add_f32_e32 v64, v64, v65
	v_mul_f32_e32 v65, 0x4f800000, v64
	v_cmp_gt_f32_e32 vcc, s0, v64
	v_mov_b32_e32 v70, v58
	v_mov_b32_e32 v71, v50
	v_cndmask_b32_e32 v64, v64, v65, vcc
	v_sqrt_f32_e32 v65, v64
	s_waitcnt vmcnt(0)
	s_mul_i32 s16, s24, 0x1400
	s_add_u32 s16, s6, s16
	s_addc_u32 s17, s7, 0
	s_add_u32 s18, s16, 0x1000
	s_addc_u32 s19, s17, 0
	v_lshlrev_b32_e32 v122, 2, v100
	global_load_dword v103, v122, s[16:17]
	global_load_dword v104, v122, s[16:17] offset:256
	global_load_dword v105, v122, s[16:17] offset:512
	global_load_dword v106, v122, s[16:17] offset:768
	global_load_dword v107, v122, s[16:17] offset:1024
	global_load_dword v108, v122, s[16:17] offset:1280
	global_load_dword v109, v122, s[16:17] offset:1536
	global_load_dword v110, v122, s[16:17] offset:1792
	global_load_dword v111, v122, s[16:17] offset:2048
	global_load_dword v112, v122, s[16:17] offset:2304
	global_load_dword v113, v122, s[16:17] offset:2560
	global_load_dword v114, v122, s[16:17] offset:2816
	global_load_dword v115, v122, s[16:17] offset:3072
	global_load_dword v116, v122, s[16:17] offset:3328
	global_load_dword v117, v122, s[16:17] offset:3584
	global_load_dword v118, v122, s[16:17] offset:3840
	global_load_dword v119, v122, s[18:19]
	global_load_dword v120, v122, s[18:19] offset:256
	global_load_dword v121, v122, s[18:19] offset:512
	global_load_dword v122, v122, s[18:19] offset:768
	v_mov_b32_e32 v72, v59
	v_mov_b32_e32 v73, v51
	v_mov_b32_e32 v74, v41
	v_add_u32_e32 v66, -1, v65
	v_fma_f32 v67, -v66, v65, v64
	v_cmp_ge_f32_e64 s[0:1], 0, v67
	v_add_u32_e32 v67, 1, v65
	v_mov_b32_e32 v75, v33
	v_cndmask_b32_e64 v66, v65, v66, s[0:1]
	v_fma_f32 v65, -v67, v65, v64
	v_cmp_lt_f32_e64 s[0:1], 0, v65
	v_mov_b32_e32 v76, v43
	v_mov_b32_e32 v77, v35
	v_cndmask_b32_e64 v65, v66, v67, s[0:1]
	v_mul_f32_e32 v66, 0x37800000, v65
	v_cndmask_b32_e32 v65, v65, v66, vcc
	v_mov_b32_e32 v66, 0x260
	v_cmp_class_f32_e32 vcc, v64, v66
	v_mov_b32_e32 v78, v25
	v_mov_b32_e32 v79, v17
	v_cndmask_b32_e32 v64, v65, v64, vcc
	v_add_f32_e32 v64, 0x322bcc77, v64
	v_div_scale_f32 v65, s[0:1], v64, v64, 1.0
	v_rcp_f32_e32 v66, v65
	s_mul_i32 s0, s23, 0x180
	s_add_i32 s8, s10, s0
	s_mov_b32 s0, 0x3a83126f
	v_fma_f32 v67, -v65, v66, 1.0
	v_fmac_f32_e32 v66, v67, v66
	v_div_scale_f32 v67, vcc, 1.0, v64, 1.0
	v_mul_f32_e32 v68, v67, v66
	v_fma_f32 v69, -v65, v68, v67
	v_fmac_f32_e32 v68, v69, v66
	v_fma_f32 v65, -v65, v68, v67
	v_div_fmas_f32 v65, v65, v66, v68
	v_div_fixup_f32 v64, v65, v64, 1.0
	v_lshl_add_u32 v65, v100, 2, s10
	ds_write_b32 v65, v64 offset:8832
	v_mov_b32_e32 v64, v60
	v_mov_b32_e32 v65, v52
	v_mov_b32_e32 v66, v56
	v_mov_b32_e32 v67, v48
	v_pk_add_f32 v[64:65], v[64:65], v[66:67]
	v_mov_b32_e32 v66, v61
	v_mov_b32_e32 v67, v53
	v_mov_b32_e32 v68, v57
	v_mov_b32_e32 v69, v49
	v_pk_add_f32 v[66:67], v[66:67], v[68:69]
	v_add_f32_e32 v64, v64, v65
	v_add_f32_e32 v65, v66, v67
	v_mov_b32_e32 v66, v62
	v_mov_b32_e32 v67, v54
	v_pk_add_f32 v[66:67], v[66:67], v[70:71]
	v_mov_b32_e32 v70, v63
	v_mov_b32_e32 v71, v55
	v_pk_add_f32 v[70:71], v[70:71], v[72:73]
	v_add_f32_dpp v64, v64, v64 row_ror:8 row_mask:0xf bank_mask:0xf bound_ctrl:1
	v_add_f32_dpp v65, v65, v65 row_ror:8 row_mask:0xf bank_mask:0xf bound_ctrl:1
	v_add_f32_e32 v66, v66, v67
	v_add_f32_e32 v67, v70, v71
	v_add_f32_dpp v64, v64, v64 row_ror:4 row_mask:0xf bank_mask:0xf bound_ctrl:1
	v_add_f32_dpp v65, v65, v65 row_ror:4 row_mask:0xf bank_mask:0xf bound_ctrl:1
	v_add_f32_dpp v66, v66, v66 row_ror:8 row_mask:0xf bank_mask:0xf bound_ctrl:1
	v_add_f32_dpp v67, v67, v67 row_ror:8 row_mask:0xf bank_mask:0xf bound_ctrl:1
	v_add_f32_dpp v64, v64, v64 row_ror:2 row_mask:0xf bank_mask:0xf bound_ctrl:1
	v_add_f32_dpp v65, v65, v65 row_ror:2 row_mask:0xf bank_mask:0xf bound_ctrl:1
	v_add_f32_dpp v66, v66, v66 row_ror:4 row_mask:0xf bank_mask:0xf bound_ctrl:1
	v_add_f32_dpp v67, v67, v67 row_ror:4 row_mask:0xf bank_mask:0xf bound_ctrl:1
	v_add_f32_dpp v64, v64, v64 row_ror:1 row_mask:0xf bank_mask:0xf bound_ctrl:1
	v_add_f32_dpp v65, v65, v65 row_ror:1 row_mask:0xf bank_mask:0xf bound_ctrl:1
	v_add_f32_dpp v66, v66, v66 row_ror:2 row_mask:0xf bank_mask:0xf bound_ctrl:1
	v_add_f32_dpp v67, v67, v67 row_ror:2 row_mask:0xf bank_mask:0xf bound_ctrl:1
	v_mul_f32_e32 v64, 0x3c800000, v64
	v_mul_f32_e32 v65, 0x3c800000, v65
	v_add_f32_dpp v66, v66, v66 row_ror:1 row_mask:0xf bank_mask:0xf bound_ctrl:1
	v_add_f32_dpp v67, v67, v67 row_ror:1 row_mask:0xf bank_mask:0xf bound_ctrl:1
	v_max_f32_e32 v64, 0, v64
	v_max_f32_e32 v65, 0, v65
	v_mul_f32_e32 v66, 0x3c800000, v66
	v_mul_f32_e32 v67, 0x3c800000, v67
	v_pk_add_f32 v[64:65], v[64:65], s[0:1] op_sel_hi:[1,0]
	v_max_f32_e32 v66, 0, v66
	v_max_f32_e32 v67, 0, v67
	v_pk_add_f32 v[68:69], v[64:65], v[64:65] op_sel:[0,1] op_sel_hi:[1,0]
	v_pk_add_f32 v[66:67], v[66:67], s[0:1] op_sel_hi:[1,0]
	v_mov_b32_e32 v72, v40
	v_pk_add_f32 v[68:69], v[68:69], v[66:67]
	v_mov_b32_e32 v73, v32
	v_pk_add_f32 v[70:71], v[68:69], v[66:67] op_sel:[0,1] op_sel_hi:[1,0]
	v_mov_b32_e32 v68, v44
	v_mov_b32_e32 v69, v36
	v_pk_add_f32 v[68:69], v[68:69], v[72:73]
	v_mov_b32_e32 v72, v45
	v_mov_b32_e32 v73, v37
	v_pk_add_f32 v[72:73], v[72:73], v[74:75]
	v_add_f32_e32 v68, v68, v69
	v_add_f32_e32 v69, v72, v73
	v_mov_b32_e32 v74, v42
	v_add_f32_dpp v68, v68, v68 row_ror:8 row_mask:0xf bank_mask:0xf bound_ctrl:1
	v_add_f32_dpp v69, v69, v69 row_ror:8 row_mask:0xf bank_mask:0xf bound_ctrl:1
	v_mov_b32_e32 v75, v34
	v_add_f32_dpp v68, v68, v68 row_ror:4 row_mask:0xf bank_mask:0xf bound_ctrl:1
	v_add_f32_dpp v69, v69, v69 row_ror:4 row_mask:0xf bank_mask:0xf bound_ctrl:1
	v_mov_b32_e32 v80, v27
	v_add_f32_dpp v68, v68, v68 row_ror:2 row_mask:0xf bank_mask:0xf bound_ctrl:1
	v_add_f32_dpp v69, v69, v69 row_ror:2 row_mask:0xf bank_mask:0xf bound_ctrl:1
	v_mov_b32_e32 v81, v19
	v_add_f32_dpp v68, v68, v68 row_ror:1 row_mask:0xf bank_mask:0xf bound_ctrl:1
	v_add_f32_dpp v69, v69, v69 row_ror:1 row_mask:0xf bank_mask:0xf bound_ctrl:1
	v_mul_f32_e32 v68, 0x3c800000, v68
	v_mul_f32_e32 v69, 0x3c800000, v69
	v_max_f32_e32 v68, 0, v68
	v_max_f32_e32 v69, 0, v69
	v_pk_add_f32 v[68:69], v[68:69], s[0:1] op_sel_hi:[1,0]
	v_mov_b32_e32 v82, v9
	v_pk_add_f32 v[70:71], v[70:71], v[68:69]
	v_mov_b32_e32 v83, v1
	v_pk_add_f32 v[72:73], v[70:71], v[68:69] op_sel:[0,1] op_sel_hi:[1,0]
	v_mov_b32_e32 v70, v46
	v_mov_b32_e32 v71, v38
	v_pk_add_f32 v[70:71], v[70:71], v[74:75]
	v_mov_b32_e32 v74, v47
	v_mov_b32_e32 v75, v39
	v_pk_add_f32 v[74:75], v[74:75], v[76:77]
	v_add_f32_e32 v70, v70, v71
	v_add_f32_e32 v71, v74, v75
	v_mov_b32_e32 v76, v24
	v_add_f32_dpp v70, v70, v70 row_ror:8 row_mask:0xf bank_mask:0xf bound_ctrl:1
	v_add_f32_dpp v71, v71, v71 row_ror:8 row_mask:0xf bank_mask:0xf bound_ctrl:1
	v_mov_b32_e32 v77, v16
	v_add_f32_dpp v70, v70, v70 row_ror:4 row_mask:0xf bank_mask:0xf bound_ctrl:1
	v_add_f32_dpp v71, v71, v71 row_ror:4 row_mask:0xf bank_mask:0xf bound_ctrl:1
	v_mov_b32_e32 v84, v11
	v_add_f32_dpp v70, v70, v70 row_ror:2 row_mask:0xf bank_mask:0xf bound_ctrl:1
	v_add_f32_dpp v71, v71, v71 row_ror:2 row_mask:0xf bank_mask:0xf bound_ctrl:1
	v_mov_b32_e32 v85, v3
	v_add_f32_dpp v70, v70, v70 row_ror:1 row_mask:0xf bank_mask:0xf bound_ctrl:1
	v_add_f32_dpp v71, v71, v71 row_ror:1 row_mask:0xf bank_mask:0xf bound_ctrl:1
	v_mul_f32_e32 v70, 0x3c800000, v70
	v_mul_f32_e32 v71, 0x3c800000, v71
	v_max_f32_e32 v70, 0, v70
	v_max_f32_e32 v71, 0, v71
	v_pk_add_f32 v[70:71], v[70:71], s[0:1] op_sel_hi:[1,0]
	v_cmp_eq_u32_e32 vcc, 0, v101
	v_pk_add_f32 v[72:73], v[72:73], v[70:71]
	s_nop 0
	v_pk_add_f32 v[74:75], v[72:73], v[70:71] op_sel:[0,1] op_sel_hi:[1,0]
	v_mov_b32_e32 v72, v28
	v_mov_b32_e32 v73, v20
	v_pk_add_f32 v[72:73], v[72:73], v[76:77]
	v_mov_b32_e32 v76, v29
	v_mov_b32_e32 v77, v21
	v_pk_add_f32 v[76:77], v[76:77], v[78:79]
	v_add_f32_e32 v72, v72, v73
	v_add_f32_e32 v73, v76, v77
	v_mov_b32_e32 v78, v26
	v_add_f32_dpp v72, v72, v72 row_ror:8 row_mask:0xf bank_mask:0xf bound_ctrl:1
	v_add_f32_dpp v73, v73, v73 row_ror:8 row_mask:0xf bank_mask:0xf bound_ctrl:1
	v_mov_b32_e32 v79, v18
	v_add_f32_dpp v72, v72, v72 row_ror:4 row_mask:0xf bank_mask:0xf bound_ctrl:1
	v_add_f32_dpp v73, v73, v73 row_ror:4 row_mask:0xf bank_mask:0xf bound_ctrl:1
	s_nop 0
	v_add_f32_dpp v72, v72, v72 row_ror:2 row_mask:0xf bank_mask:0xf bound_ctrl:1
	v_add_f32_dpp v73, v73, v73 row_ror:2 row_mask:0xf bank_mask:0xf bound_ctrl:1
	s_nop 0
	v_add_f32_dpp v72, v72, v72 row_ror:1 row_mask:0xf bank_mask:0xf bound_ctrl:1
	v_add_f32_dpp v73, v73, v73 row_ror:1 row_mask:0xf bank_mask:0xf bound_ctrl:1
	v_mul_f32_e32 v72, 0x3c800000, v72
	v_mul_f32_e32 v73, 0x3c800000, v73
	v_max_f32_e32 v72, 0, v72
	v_max_f32_e32 v73, 0, v73
	v_pk_add_f32 v[72:73], v[72:73], s[0:1] op_sel_hi:[1,0]
	s_nop 0
	v_pk_add_f32 v[74:75], v[74:75], v[72:73]
	s_nop 0
	v_pk_add_f32 v[76:77], v[74:75], v[72:73] op_sel:[0,1] op_sel_hi:[1,0]
	v_mov_b32_e32 v74, v30
	v_mov_b32_e32 v75, v22
	v_pk_add_f32 v[74:75], v[74:75], v[78:79]
	v_mov_b32_e32 v78, v31
	v_mov_b32_e32 v79, v23
	v_pk_add_f32 v[78:79], v[78:79], v[80:81]
	v_add_f32_e32 v74, v74, v75
	v_add_f32_e32 v75, v78, v79
	v_mov_b32_e32 v80, v8
	v_add_f32_dpp v74, v74, v74 row_ror:8 row_mask:0xf bank_mask:0xf bound_ctrl:1
	v_add_f32_dpp v75, v75, v75 row_ror:8 row_mask:0xf bank_mask:0xf bound_ctrl:1
	v_mov_b32_e32 v81, v0
	v_add_f32_dpp v74, v74, v74 row_ror:4 row_mask:0xf bank_mask:0xf bound_ctrl:1
	v_add_f32_dpp v75, v75, v75 row_ror:4 row_mask:0xf bank_mask:0xf bound_ctrl:1
	s_nop 0
	v_add_f32_dpp v74, v74, v74 row_ror:2 row_mask:0xf bank_mask:0xf bound_ctrl:1
	v_add_f32_dpp v75, v75, v75 row_ror:2 row_mask:0xf bank_mask:0xf bound_ctrl:1
	s_nop 0
	v_add_f32_dpp v74, v74, v74 row_ror:1 row_mask:0xf bank_mask:0xf bound_ctrl:1
	v_add_f32_dpp v75, v75, v75 row_ror:1 row_mask:0xf bank_mask:0xf bound_ctrl:1
	v_mul_f32_e32 v74, 0x3c800000, v74
	v_mul_f32_e32 v75, 0x3c800000, v75
	v_max_f32_e32 v74, 0, v74
	v_max_f32_e32 v75, 0, v75
	v_pk_add_f32 v[74:75], v[74:75], s[0:1] op_sel_hi:[1,0]
	s_nop 0
	v_pk_add_f32 v[76:77], v[76:77], v[74:75]
	s_nop 0
	v_pk_add_f32 v[78:79], v[76:77], v[74:75] op_sel:[0,1] op_sel_hi:[1,0]
	v_mov_b32_e32 v76, v12
	v_mov_b32_e32 v77, v4
	v_pk_add_f32 v[76:77], v[76:77], v[80:81]
	v_mov_b32_e32 v80, v13
	v_mov_b32_e32 v81, v5
	v_pk_add_f32 v[80:81], v[80:81], v[82:83]
	v_add_f32_e32 v76, v76, v77
	v_add_f32_e32 v77, v80, v81
	v_mov_b32_e32 v82, v10
	v_add_f32_dpp v76, v76, v76 row_ror:8 row_mask:0xf bank_mask:0xf bound_ctrl:1
	v_add_f32_dpp v77, v77, v77 row_ror:8 row_mask:0xf bank_mask:0xf bound_ctrl:1
	v_mov_b32_e32 v83, v2
	v_add_f32_dpp v76, v76, v76 row_ror:4 row_mask:0xf bank_mask:0xf bound_ctrl:1
	v_add_f32_dpp v77, v77, v77 row_ror:4 row_mask:0xf bank_mask:0xf bound_ctrl:1
	s_nop 0
	v_add_f32_dpp v76, v76, v76 row_ror:2 row_mask:0xf bank_mask:0xf bound_ctrl:1
	v_add_f32_dpp v77, v77, v77 row_ror:2 row_mask:0xf bank_mask:0xf bound_ctrl:1
	s_nop 0
	v_add_f32_dpp v76, v76, v76 row_ror:1 row_mask:0xf bank_mask:0xf bound_ctrl:1
	v_add_f32_dpp v77, v77, v77 row_ror:1 row_mask:0xf bank_mask:0xf bound_ctrl:1
	v_mul_f32_e32 v76, 0x3c800000, v76
	v_mul_f32_e32 v77, 0x3c800000, v77
	v_max_f32_e32 v76, 0, v76
	v_max_f32_e32 v77, 0, v77
	v_pk_add_f32 v[76:77], v[76:77], s[0:1] op_sel_hi:[1,0]
	s_nop 0
	v_pk_add_f32 v[78:79], v[78:79], v[76:77]
	s_nop 0
	v_pk_add_f32 v[80:81], v[78:79], v[76:77] op_sel:[0,1] op_sel_hi:[1,0]
	v_mov_b32_e32 v78, v14
	v_mov_b32_e32 v79, v6
	v_pk_add_f32 v[78:79], v[78:79], v[82:83]
	v_mov_b32_e32 v82, v15
	v_mov_b32_e32 v83, v7
	v_pk_add_f32 v[82:83], v[82:83], v[84:85]
	v_add_f32_e32 v78, v78, v79
	v_add_f32_e32 v79, v82, v83
	s_nop 0
	v_add_f32_dpp v78, v78, v78 row_ror:8 row_mask:0xf bank_mask:0xf bound_ctrl:1
	v_add_f32_dpp v79, v79, v79 row_ror:8 row_mask:0xf bank_mask:0xf bound_ctrl:1
	s_nop 0
	v_add_f32_dpp v78, v78, v78 row_ror:4 row_mask:0xf bank_mask:0xf bound_ctrl:1
	v_add_f32_dpp v79, v79, v79 row_ror:4 row_mask:0xf bank_mask:0xf bound_ctrl:1
	s_nop 0
	v_add_f32_dpp v78, v78, v78 row_ror:2 row_mask:0xf bank_mask:0xf bound_ctrl:1
	v_add_f32_dpp v79, v79, v79 row_ror:2 row_mask:0xf bank_mask:0xf bound_ctrl:1
	s_nop 0
	v_add_f32_dpp v78, v78, v78 row_ror:1 row_mask:0xf bank_mask:0xf bound_ctrl:1
	v_add_f32_dpp v79, v79, v79 row_ror:1 row_mask:0xf bank_mask:0xf bound_ctrl:1
	v_mul_f32_e32 v78, 0x3c800000, v78
	v_mul_f32_e32 v79, 0x3c800000, v79
	v_max_f32_e32 v78, 0, v78
	v_max_f32_e32 v79, 0, v79
	v_pk_add_f32 v[78:79], v[78:79], s[0:1] op_sel_hi:[1,0]
	s_nop 0
	v_pk_add_f32 v[80:81], v[80:81], v[78:79]
	s_nop 0
	v_pk_add_f32 v[80:81], v[80:81], v[78:79] op_sel:[0,1] op_sel_hi:[1,0]
	s_nop 0
	v_mov_b32_e32 v81, v80
	s_nop 1
	v_permlane16_swap_b32_e32 v80, v81
	v_add_f32_e32 v80, v80, v81
	v_mov_b32_e32 v81, v80
	s_nop 1
	v_permlane32_swap_b32_e32 v80, v81
	s_and_saveexec_b64 s[0:1], vcc
	s_cbranch_execz .LBB1_34
	v_add_f32_e32 v80, v80, v81
	v_div_scale_f32 v81, s[2:3], v80, v80, 1.0
	v_rcp_f32_e32 v82, v81
	v_div_scale_f32 v83, vcc, 1.0, v80, 1.0
	v_fma_f32 v84, -v81, v82, 1.0
	v_fmac_f32_e32 v82, v84, v82
	v_mul_f32_e32 v84, v83, v82
	v_fma_f32 v85, -v81, v84, v83
	v_fmac_f32_e32 v84, v85, v82
	v_fma_f32 v81, -v81, v84, v83
	v_div_fmas_f32 v81, v81, v82, v84
	v_div_fixup_f32 v80, v81, v80, 1.0
	v_add_u32_e32 v81, s8, v100
	v_pk_mul_f32 v[64:65], v[80:81], v[64:65] op_sel_hi:[0,1]
	v_pk_mul_f32 v[66:67], v[80:81], v[66:67] op_sel_hi:[0,1]
	ds_write_b128 v81, v[64:67] offset:5632
	v_pk_mul_f32 v[64:65], v[80:81], v[68:69] op_sel_hi:[0,1]
	v_pk_mul_f32 v[66:67], v[80:81], v[70:71] op_sel_hi:[0,1]
	ds_write_b128 v81, v[64:67] offset:5696
	v_pk_mul_f32 v[64:65], v[80:81], v[72:73] op_sel_hi:[0,1]
	v_pk_mul_f32 v[66:67], v[80:81], v[74:75] op_sel_hi:[0,1]
	ds_write_b128 v81, v[64:67] offset:5760
	v_pk_mul_f32 v[64:65], v[80:81], v[76:77] op_sel_hi:[0,1]
	v_pk_mul_f32 v[66:67], v[80:81], v[78:79] op_sel_hi:[0,1]
	ds_write_b128 v81, v[64:67] offset:5824

.LBB1_36:
	s_or_b64 exec, exec, s[2:3]
	s_waitcnt vmcnt(0)
	v_add_f32_e32 v103, 0, v103
	v_add_f32_e32 v103, v103, v104
	v_add_f32_e32 v103, v103, v105
	v_add_f32_e32 v103, v103, v106
	v_add_f32_e32 v103, v103, v107
	v_add_f32_e32 v103, v103, v108
	v_add_f32_e32 v103, v103, v109
	v_add_f32_e32 v103, v103, v110
	v_add_f32_e32 v103, v103, v111
	v_add_f32_e32 v103, v103, v112
	v_add_f32_e32 v103, v103, v113
	v_add_f32_e32 v103, v103, v114
	v_add_f32_e32 v103, v103, v115
	v_add_f32_e32 v103, v103, v116
	v_add_f32_e32 v103, v103, v117
	v_add_f32_e32 v103, v103, v118
	v_add_f32_e32 v103, v103, v119
	v_add_f32_e32 v103, v103, v120
	v_add_f32_e32 v103, v103, v121
	v_add_f32_e32 v103, v103, v122
	s_mov_b32 s14, 0xf800000
	s_mov_b32 s11, 0x41e6d4ca
	v_cmp_gt_f32_e32 vcc, s14, v103
	v_mul_f32_e32 v104, 0x4f800000, v103
	s_nop 0
	v_cndmask_b32_e32 v104, v103, v104, vcc
	v_sqrt_f32_e32 v103, v104
	s_nop 0
	v_add_u32_e32 v105, -1, v103
	v_fma_f32 v108, -v105, v103, v104
	v_cmp_ge_f32_e64 s[2:3], 0, v108
	v_add_u32_e32 v108, 1, v103
	s_nop 0
	v_cndmask_b32_e64 v105, v103, v105, s[2:3]
	v_fma_f32 v103, -v108, v103, v104
	v_cmp_lt_f32_e64 s[2:3], 0, v103
	s_nop 1
	v_cndmask_b32_e64 v103, v105, v108, s[2:3]
	v_mul_f32_e32 v105, 0x37800000, v103
	v_cndmask_b32_e32 v105, v103, v105, vcc
	v_mov_b32_e32 v103, 0x260
	v_cmp_class_f32_e32 vcc, v104, v103
	s_nop 1
	v_cndmask_b32_e32 v104, v105, v104, vcc
	v_add_f32_e32 v104, 0x322bcc77, v104
	v_div_scale_f32 v108, s[2:3], v104, v104, s11
	v_rcp_f32_e32 v105, v108
	s_nop 0
	v_fma_f32 v109, -v108, v105, 1.0
	v_fmac_f32_e32 v105, v109, v105
	v_div_scale_f32 v107, vcc, s11, v104, s11
	v_mul_f32_e32 v106, v107, v105
	v_fma_f32 v111, -v108, v106, v107
	v_fmac_f32_e32 v106, v111, v105
	v_fma_f32 v107, -v108, v106, v107
	s_nop 0
	v_div_fmas_f32 v109, v107, v105, v106
	v_div_fixup_f32 v109, v109, v104, s11
	v_lshlrev_b32_e32 v110, 2, v101
	ds_bpermute_b32 v64, v110, v109
	ds_bpermute_b32 v65, v110, v109 offset:64
	ds_bpermute_b32 v68, v110, v109 offset:128
	ds_bpermute_b32 v70, v110, v109 offset:192
	s_mul_i32 s2, s23, 0x1f80
	s_add_i32 s6, s8, s2
	s_movk_i32 s2, 0x88
	v_and_b32_e32 v66, 0x70, v100
	v_add_u32_e32 v71, s10, v66
	ds_read_b128 v[76:79], v71 offset:8832
	v_lshrrev_b32_e32 v67, 4, v100
	v_lshlrev_b32_e32 v67, 3, v67
	v_add_u32_e32 v72, s6, v67
	s_waitcnt lgkmcnt(0)
	v_mul_f32_e32 v73, v76, v64
	v_fmaak_f32 v60, v60, v73, 0xc1e6d4ca
	v_exp_f32_e32 v73, v60
	v_mul_f32_e32 v60, v77, v64
	v_fmaak_f32 v60, v61, v60, 0xc1e6d4ca
	v_mul_f32_e32 v61, v78, v64
	v_fmaak_f32 v61, v62, v61, 0xc1e6d4ca
	v_mul_f32_e32 v62, v79, v64
	v_fmaak_f32 v62, v63, v62, 0xc1e6d4ca
	v_exp_f32_e32 v61, v61
	v_exp_f32_e32 v62, v62
	v_exp_f32_e32 v74, v60
	v_mad_u32_u24 v60, v101, s2, v72
	s_mov_b32 s10, s9
	v_cvt_pk_bf16_f32 v63, v61, v62
	v_mul_f32_e32 v61, v76, v65
	v_fmaak_f32 v56, v56, v61, 0xc1e6d4ca
	v_mul_f32_e32 v61, v77, v65
	v_fmaak_f32 v57, v57, v61, 0xc1e6d4ca
	v_exp_f32_e32 v61, v57
	v_mul_f32_e32 v57, v78, v65
	v_cvt_pk_bf16_f32 v62, v73, v74
	v_fmaak_f32 v57, v58, v57, 0xc1e6d4ca
	ds_write_b64 v60, v[62:63] offset:10240
	v_exp_f32_e32 v62, v57
	v_mul_f32_e32 v57, v79, v65
	v_fmaak_f32 v57, v59, v57, 0xc1e6d4ca
	v_exp_f32_e32 v56, v56
	v_exp_f32_e32 v59, v57
	v_mov_b32_e32 v57, 0x880
	v_mad_u32_u24 v57, v101, s2, v57
	v_add_u32_e32 v58, v72, v57
	v_cvt_pk_bf16_f32 v63, v62, v59
	v_cvt_pk_bf16_f32 v62, v56, v61
	v_mul_f32_e32 v56, v76, v68
	v_fmaak_f32 v52, v52, v56, 0xc1e6d4ca
	v_exp_f32_e32 v56, v52
	v_mul_f32_e32 v52, v77, v68
	v_fmaak_f32 v52, v53, v52, 0xc1e6d4ca
	v_exp_f32_e32 v59, v52
	v_mul_f32_e32 v52, v78, v68
	v_fmaak_f32 v52, v54, v52, 0xc1e6d4ca
	v_exp_f32_e32 v54, v52
	v_mul_f32_e32 v52, v79, v68
	v_fmaak_f32 v52, v55, v52, 0xc1e6d4ca
	v_exp_f32_e32 v55, v52
	v_mov_b32_e32 v52, 0x1100
	v_mad_u32_u24 v52, v101, s2, v52
	v_add_u32_e32 v53, v72, v52
	v_cvt_pk_bf16_f32 v55, v54, v55
	v_cvt_pk_bf16_f32 v54, v56, v59
	ds_write_b64 v53, v[54:55] offset:10240
	v_mul_f32_e32 v54, v76, v70
	v_fmaak_f32 v48, v48, v54, 0xc1e6d4ca
	v_exp_f32_e32 v54, v48
	v_mul_f32_e32 v48, v77, v70
	v_fmaak_f32 v48, v49, v48, 0xc1e6d4ca
	v_exp_f32_e32 v49, v48
	v_mul_f32_e32 v48, v78, v70
	v_fmaak_f32 v48, v50, v48, 0xc1e6d4ca
	v_exp_f32_e32 v50, v48
	v_mul_f32_e32 v48, v79, v70
	v_fmaak_f32 v48, v51, v48, 0xc1e6d4ca
	v_exp_f32_e32 v51, v48
	v_mov_b32_e32 v48, 0x1980
	v_mad_u32_u24 v56, v101, s2, v48
	v_add_u32_e32 v48, v72, v56
	v_cvt_pk_bf16_f32 v51, v50, v51
	v_cvt_pk_bf16_f32 v50, v54, v49
	ds_write_b64 v58, v[62:63] offset:10240
	ds_write_b64 v48, v[50:51] offset:10240
	ds_read_b128 v[76:79], v71 offset:8896
	s_mov_b32 s11, s9
	s_waitcnt lgkmcnt(0)
	v_mul_f32_e32 v49, v76, v64
	v_fmaak_f32 v44, v44, v49, 0xc1e6d4ca
	v_mul_f32_e32 v49, v78, v64
	v_fmaak_f32 v46, v46, v49, 0xc1e6d4ca
	v_mul_f32_e32 v49, v79, v64
	v_fmaak_f32 v47, v47, v49, 0xc1e6d4ca
	v_exp_f32_e32 v46, v46
	v_exp_f32_e32 v47, v47
	v_mul_f32_e32 v49, v77, v64
	v_fmaak_f32 v45, v45, v49, 0xc1e6d4ca
	v_exp_f32_e32 v49, v45
	v_cvt_pk_bf16_f32 v45, v46, v47
	v_mul_f32_e32 v46, v76, v65
	v_fmaak_f32 v40, v40, v46, 0xc1e6d4ca
	v_mul_f32_e32 v46, v77, v65
	v_fmaak_f32 v41, v41, v46, 0xc1e6d4ca
	v_mul_f32_e32 v46, v78, v65
	v_fmaak_f32 v42, v42, v46, 0xc1e6d4ca
	v_mul_f32_e32 v46, v79, v65
	v_fmaak_f32 v43, v43, v46, 0xc1e6d4ca
	v_exp_f32_e32 v40, v40
	v_exp_f32_e32 v42, v42
	v_exp_f32_e32 v43, v43
	v_exp_f32_e32 v46, v41
	v_exp_f32_e32 v44, v44
	v_cvt_pk_bf16_f32 v41, v42, v43
	v_cvt_pk_bf16_f32 v40, v40, v46
	ds_write_b64 v58, v[40:41] offset:10272
	v_mul_f32_e32 v40, v76, v68
	v_fmaak_f32 v36, v36, v40, 0xc1e6d4ca
	v_mul_f32_e32 v40, v78, v68
	v_fmaak_f32 v38, v38, v40, 0xc1e6d4ca
	v_mul_f32_e32 v40, v79, v68
	v_fmaak_f32 v39, v39, v40, 0xc1e6d4ca
	v_exp_f32_e32 v38, v38
	v_exp_f32_e32 v39, v39
	v_mul_f32_e32 v40, v77, v68
	v_fmaak_f32 v37, v37, v40, 0xc1e6d4ca
	v_exp_f32_e32 v40, v37
	v_cvt_pk_bf16_f32 v37, v38, v39
	v_mul_f32_e32 v38, v76, v70
	v_fmaak_f32 v32, v32, v38, 0xc1e6d4ca
	v_mul_f32_e32 v38, v77, v70
	v_fmaak_f32 v33, v33, v38, 0xc1e6d4ca
	v_mul_f32_e32 v38, v78, v70
	v_fmaak_f32 v34, v34, v38, 0xc1e6d4ca
	v_mul_f32_e32 v38, v79, v70
	v_fmaak_f32 v35, v35, v38, 0xc1e6d4ca
	v_exp_f32_e32 v36, v36
	v_exp_f32_e32 v32, v32
	v_exp_f32_e32 v34, v34
	v_exp_f32_e32 v35, v35
	v_exp_f32_e32 v38, v33
	v_cvt_pk_bf16_f32 v44, v44, v49
	v_cvt_pk_bf16_f32 v36, v36, v40
	v_cvt_pk_bf16_f32 v33, v34, v35
	v_cvt_pk_bf16_f32 v32, v32, v38
	ds_write_b64 v60, v[44:45] offset:10272
	ds_write_b64 v53, v[36:37] offset:10272
	ds_write_b64 v48, v[32:33] offset:10272
	ds_read_b128 v[32:35], v71 offset:8960
	s_waitcnt lgkmcnt(0)
	v_mul_f32_e32 v36, v32, v64
	v_fmaak_f32 v28, v28, v36, 0xc1e6d4ca
	v_mul_f32_e32 v36, v34, v64
	v_fmaak_f32 v30, v30, v36, 0xc1e6d4ca
	v_mul_f32_e32 v36, v35, v64
	v_fmaak_f32 v31, v31, v36, 0xc1e6d4ca
	v_exp_f32_e32 v30, v30
	v_exp_f32_e32 v31, v31
	v_mul_f32_e32 v36, v33, v64
	v_fmaak_f32 v29, v29, v36, 0xc1e6d4ca
	v_exp_f32_e32 v36, v29
	v_cvt_pk_bf16_f32 v29, v30, v31
	v_mul_f32_e32 v30, v32, v65
	v_fmaak_f32 v24, v24, v30, 0xc1e6d4ca
	v_mul_f32_e32 v30, v33, v65
	v_fmaak_f32 v25, v25, v30, 0xc1e6d4ca
	v_mul_f32_e32 v30, v34, v65
	v_fmaak_f32 v26, v26, v30, 0xc1e6d4ca
	v_mul_f32_e32 v30, v35, v65
	v_fmaak_f32 v27, v27, v30, 0xc1e6d4ca
	v_exp_f32_e32 v24, v24
	v_exp_f32_e32 v26, v26
	v_exp_f32_e32 v27, v27
	v_exp_f32_e32 v30, v25
	v_exp_f32_e32 v28, v28
	v_cvt_pk_bf16_f32 v25, v26, v27
	v_cvt_pk_bf16_f32 v24, v24, v30
	ds_write_b64 v58, v[24:25] offset:10304
	v_mul_f32_e32 v24, v32, v68
	v_fmaak_f32 v20, v20, v24, 0xc1e6d4ca
	v_mul_f32_e32 v24, v34, v68
	v_fmaak_f32 v22, v22, v24, 0xc1e6d4ca
	v_mul_f32_e32 v24, v35, v68
	v_fmaak_f32 v23, v23, v24, 0xc1e6d4ca
	v_exp_f32_e32 v22, v22
	v_exp_f32_e32 v23, v23
	v_mul_f32_e32 v24, v33, v68
	v_fmaak_f32 v21, v21, v24, 0xc1e6d4ca
	v_exp_f32_e32 v24, v21
	v_cvt_pk_bf16_f32 v21, v22, v23
	v_mul_f32_e32 v22, v32, v70
	v_fmaak_f32 v16, v16, v22, 0xc1e6d4ca
	v_mul_f32_e32 v22, v33, v70
	v_fmaak_f32 v17, v17, v22, 0xc1e6d4ca
	v_mul_f32_e32 v22, v34, v70
	v_fmaak_f32 v18, v18, v22, 0xc1e6d4ca
	v_mul_f32_e32 v22, v35, v70
	v_fmaak_f32 v19, v19, v22, 0xc1e6d4ca
	v_exp_f32_e32 v20, v20
	v_exp_f32_e32 v16, v16
	v_exp_f32_e32 v18, v18
	v_exp_f32_e32 v19, v19
	v_exp_f32_e32 v22, v17
	v_cvt_pk_bf16_f32 v28, v28, v36
	v_cvt_pk_bf16_f32 v20, v20, v24
	v_cvt_pk_bf16_f32 v17, v18, v19
	v_cvt_pk_bf16_f32 v16, v16, v22
	ds_write_b64 v60, v[28:29] offset:10304
	ds_write_b64 v53, v[20:21] offset:10304
	ds_write_b64 v48, v[16:17] offset:10304
	ds_read_b128 v[16:19], v71 offset:9024
	v_mov_b32_e32 v20, 0xc1e6d4ca
	s_waitcnt lgkmcnt(0)
	v_mul_f32_e32 v21, v16, v64
	v_fmaak_f32 v12, v12, v21, 0xc1e6d4ca
	v_mul_f32_e32 v21, v18, v64
	v_fmaak_f32 v14, v14, v21, 0xc1e6d4ca
	v_mul_f32_e32 v21, v19, v64
	v_fmaak_f32 v15, v15, v21, 0xc1e6d4ca
	v_exp_f32_e32 v14, v14
	v_exp_f32_e32 v15, v15
	v_mul_f32_e32 v21, v17, v64
	v_fmaak_f32 v13, v13, v21, 0xc1e6d4ca
	v_exp_f32_e32 v21, v13
	v_cvt_pk_bf16_f32 v13, v14, v15
	v_mul_f32_e32 v14, v16, v65
	v_fmaak_f32 v8, v8, v14, 0xc1e6d4ca
	v_mul_f32_e32 v14, v17, v65
	v_fmaak_f32 v9, v9, v14, 0xc1e6d4ca
	v_mul_f32_e32 v14, v18, v65
	v_fmaak_f32 v10, v10, v14, 0xc1e6d4ca
	v_mul_f32_e32 v14, v19, v65
	v_fmaak_f32 v11, v11, v14, 0xc1e6d4ca
	v_exp_f32_e32 v8, v8
	v_exp_f32_e32 v10, v10
	v_exp_f32_e32 v11, v11
	v_exp_f32_e32 v14, v9
	v_exp_f32_e32 v12, v12
	v_and_b32_e32 v64, 1, v100
	v_cvt_pk_bf16_f32 v9, v10, v11
	v_cvt_pk_bf16_f32 v8, v8, v14
	ds_write_b64 v58, v[8:9] offset:10336
	v_mul_f32_e32 v8, v16, v68
	v_fmaak_f32 v4, v4, v8, 0xc1e6d4ca
	v_mul_f32_e32 v8, v18, v68
	v_fmaak_f32 v6, v6, v8, 0xc1e6d4ca
	v_mul_f32_e32 v8, v19, v68
	v_fmaak_f32 v7, v7, v8, 0xc1e6d4ca
	v_exp_f32_e32 v6, v6
	v_exp_f32_e32 v7, v7
	v_mul_f32_e32 v8, v17, v68
	v_fmaak_f32 v5, v5, v8, 0xc1e6d4ca
	v_exp_f32_e32 v8, v5
	v_cvt_pk_bf16_f32 v5, v6, v7
	v_mul_f32_e32 v6, v16, v70
	v_fmaak_f32 v0, v0, v6, 0xc1e6d4ca
	v_mul_f32_e32 v6, v17, v70
	v_fmaak_f32 v1, v1, v6, 0xc1e6d4ca
	v_mul_f32_e32 v6, v18, v70
	v_fmaak_f32 v2, v2, v6, 0xc1e6d4ca
	v_mul_f32_e32 v6, v19, v70
	v_fmac_f32_e32 v20, v3, v6
	v_exp_f32_e32 v0, v0
	v_exp_f32_e32 v2, v2
	v_exp_f32_e32 v3, v20
	v_exp_f32_e32 v6, v1
	v_exp_f32_e32 v4, v4
	v_cvt_pk_bf16_f32 v12, v12, v21
	v_cvt_pk_bf16_f32 v1, v2, v3
	v_cvt_pk_bf16_f32 v0, v0, v6
	ds_write_b64 v48, v[0:1] offset:10336
	v_lshrrev_b32_e32 v0, 2, v101
	v_or_b32_e32 v0, v67, v0
	v_lshlrev_b32_e32 v1, 3, v100
	v_mul_u32_u24_e32 v0, 0x88, v0
	v_and_b32_e32 v1, 24, v1
	v_add_u32_e32 v2, s6, v66
	v_cvt_pk_bf16_f32 v4, v4, v8
	v_add3_u32 v62, s6, v0, v1
	v_mad_u32_u24 v0, v101, s2, v2
	ds_write_b64 v60, v[12:13] offset:10336
	ds_write_b64 v53, v[4:5] offset:10336
	s_movk_i32 s34, 0x88
	v_and_b32_e32 v64, 32, v100
	v_and_b32_e32 v66, 16, v100
	v_mad_u32_u24 v65, v101, s34, v64
	v_add_u32_e32 v65, s6, v65
	v_add_u32_e32 v67, v65, v66
	v_sub_u32_e32 v65, v65, v66
	v_lshrrev_b32_e32 v68, 1, v100
	v_and_b32_e32 v68, 16, v68
	v_bfe_u32 v69, v100, 2, 2
	v_or_b32_e32 v68, v68, v69
	v_and_b32_e32 v69, 3, v100
	v_lshlrev_b32_e32 v69, 3, v69
	v_mad_u32_u24 v68, v68, s34, v69
	v_add_u32_e32 v68, s6, v68
	s_movk_i32 s35, 0x44
	v_mul_u32_u24_e32 v66, s35, v66
	v_add_u32_e32 v69, v68, v66
	v_sub_u32_e32 v68, v68, v66
	ds_read_b64 v[0:1], v67 offset:10240
	ds_read_b64 v[2:3], v65 offset:10264
	ds_read_b64 v[4:5], v67 offset:10304
	ds_read_b64 v[6:7], v65 offset:10328
	ds_read_b64 v[8:9], v67 offset:12424
	ds_read_b64 v[10:11], v67 offset:12416
	ds_read_b64 v[12:13], v67 offset:12488
	ds_read_b64 v[14:15], v67 offset:12480
	ds_read_b64 v[16:17], v65 offset:14608
	ds_read_b64 v[18:19], v67 offset:14600
	ds_read_b64 v[20:21], v65 offset:14672
	ds_read_b64 v[22:23], v67 offset:14664
	ds_read_b64 v[24:25], v65 offset:16792
	ds_read_b64 v[26:27], v65 offset:16784
	ds_read_b64 v[28:29], v65 offset:16856
	ds_read_b64 v[30:31], v65 offset:16848
	ds_read_b64_tr_b16 v[32:33], v69 offset:10240
	ds_read_b64_tr_b16 v[34:35], v68 offset:11872
	ds_read_b64_tr_b16 v[36:37], v69 offset:14592
	ds_read_b64_tr_b16 v[38:39], v68 offset:16224
	ds_read_b64_tr_b16 v[40:41], v69 offset:10816
	ds_read_b64_tr_b16 v[42:43], v69 offset:10272
	ds_read_b64_tr_b16 v[44:45], v69 offset:15168
	ds_read_b64_tr_b16 v[46:47], v69 offset:14624
	ds_read_b64_tr_b16 v[48:49], v68 offset:11392
	ds_read_b64_tr_b16 v[50:51], v69 offset:10848
	ds_read_b64_tr_b16 v[52:53], v68 offset:15744
	ds_read_b64_tr_b16 v[54:55], v69 offset:15200
	ds_read_b64_tr_b16 v[56:57], v68 offset:11968
	ds_read_b64_tr_b16 v[58:59], v68 offset:11424
	ds_read_b64_tr_b16 v[60:61], v68 offset:16320
	ds_read_b64_tr_b16 v[62:63], v68 offset:15776
	ds_read2st64_b32 v[116:117], v102 offset0:22 offset1:23
	v_and_b32_e32 v110, 1, v100
	v_cmp_eq_u32_e32 vcc, 0, v110
	v_mov_b32_e32 v110, 0xeeeeeeee
	v_mov_b32_e32 v111, 0x44444444
	s_mov_b32 s32, 0x2b8cbccc
	s_mov_b32 s33, 0
	v_cndmask_b32_e32 v64, v110, v111, vcc
	v_mov_b32_e32 v68, 0x3f803f80
	v_mov_b32_e32 v69, v68
	v_mov_b32_e32 v70, v68
	v_mov_b32_e32 v71, v68
	v_mov_b64_e32 v[72:73], s[32:33]
	v_mov_b64_e32 v[76:77], s[32:33]
	v_mov_b64_e32 v[80:81], s[32:33]
	v_mov_b64_e32 v[84:85], s[32:33]
	v_mov_b64_e32 v[88:89], s[32:33]
	v_mov_b64_e32 v[92:93], s[32:33]
	v_mov_b64_e32 v[96:97], s[32:33]
	v_mov_b64_e32 v[104:105], s[32:33]
	s_movk_i32 s30, 100
	s_waitcnt lgkmcnt(0)
	v_mov_b32_dpp v112, v116 quad_perm:[0,2,0,2] row_mask:0xf bank_mask:0xf
	v_mov_b32_dpp v113, v116 quad_perm:[1,3,1,3] row_mask:0xf bank_mask:0xf
	v_mov_b32_dpp v114, v117 quad_perm:[0,2,0,2] row_mask:0xf bank_mask:0xf
	v_mov_b32_dpp v115, v117 quad_perm:[1,3,1,3] row_mask:0xf bank_mask:0xf
	v_smfmac_f32_16x16x64_bf16 v[72:75], v[68:71], v[0:7], v64
	v_smfmac_f32_16x16x64_bf16 v[76:79], v[68:71], v[8:15], v64
	v_smfmac_f32_16x16x64_bf16 v[80:83], v[68:71], v[16:23], v64
	v_smfmac_f32_16x16x64_bf16 v[84:87], v[68:71], v[24:31], v64
	s_nop 0
.Lsk_loop:
	s_nop 3
	v_add_f32_dpp v108, v72, v73 quad_perm:[0,1,2,3] row_mask:0x1 bank_mask:0xf
	v_add_f32_dpp v108, v76, v77 quad_perm:[0,1,2,3] row_mask:0x2 bank_mask:0xf
	v_add_f32_dpp v108, v80, v81 quad_perm:[0,1,2,3] row_mask:0x4 bank_mask:0xf
	v_add_f32_dpp v108, v84, v85 quad_perm:[0,1,2,3] row_mask:0x8 bank_mask:0xf
	v_rcp_f32_e32 v109, v108
	v_mov_b64_e32 v[88:89], s[32:33]
	v_mov_b64_e32 v[92:93], s[32:33]
	v_mul_f32_dpp v110, v109, v114 quad_perm:[0,2,0,2] row_mask:0xf bank_mask:0xf
	v_mul_f32_dpp v111, v109, v115 quad_perm:[1,3,1,3] row_mask:0xf bank_mask:0xf
	v_cvt_pk_bf16_f32 v68, v110, v111
	v_mov_b64_e32 v[96:97], s[32:33]
	v_mov_b64_e32 v[104:105], s[32:33]
	v_mov_b32_dpp v69, v68 row_ror:4 row_mask:0xf bank_mask:0xf
	v_mov_b32_dpp v70, v68 row_ror:8 row_mask:0xf bank_mask:0xf
	v_mov_b32_dpp v71, v68 row_ror:12 row_mask:0xf bank_mask:0xf
	s_nop 1
	v_smfmac_f32_16x16x64_bf16 v[88:91], v[68:71], v[32:39], v64
	v_smfmac_f32_16x16x64_bf16 v[92:95], v[68:71], v[40:47], v64
	v_smfmac_f32_16x16x64_bf16 v[96:99], v[68:71], v[48:55], v64
	v_smfmac_f32_16x16x64_bf16 v[104:107], v[68:71], v[56:63], v64
	s_nop 4
	v_add_f32_dpp v108, v88, v89 quad_perm:[0,1,2,3] row_mask:0x1 bank_mask:0xf
	v_add_f32_dpp v108, v92, v93 quad_perm:[0,1,2,3] row_mask:0x2 bank_mask:0xf
	v_add_f32_dpp v108, v96, v97 quad_perm:[0,1,2,3] row_mask:0x4 bank_mask:0xf
	v_add_f32_dpp v108, v104, v105 quad_perm:[0,1,2,3] row_mask:0x8 bank_mask:0xf
	v_rcp_f32_e32 v109, v108
	v_mov_b64_e32 v[72:73], s[32:33]
	v_mov_b64_e32 v[76:77], s[32:33]
	v_mul_f32_dpp v110, v109, v112 quad_perm:[0,2,0,2] row_mask:0xf bank_mask:0xf
	v_mul_f32_dpp v111, v109, v113 quad_perm:[1,3,1,3] row_mask:0xf bank_mask:0xf
	v_cvt_pk_bf16_f32 v68, v110, v111
	v_mov_b64_e32 v[80:81], s[32:33]
	v_mov_b64_e32 v[84:85], s[32:33]
	v_mov_b32_dpp v69, v68 row_ror:4 row_mask:0xf bank_mask:0xf
	v_mov_b32_dpp v70, v68 row_ror:8 row_mask:0xf bank_mask:0xf
	v_mov_b32_dpp v71, v68 row_ror:12 row_mask:0xf bank_mask:0xf
	s_add_i32 s30, s30, -1
	s_cmp_lg_u32 s30, 0
	v_smfmac_f32_16x16x64_bf16 v[72:75], v[68:71], v[0:7], v64
	v_smfmac_f32_16x16x64_bf16 v[76:79], v[68:71], v[8:15], v64
	v_smfmac_f32_16x16x64_bf16 v[80:83], v[68:71], v[16:23], v64
	v_smfmac_f32_16x16x64_bf16 v[84:87], v[68:71], v[24:31], v64
	s_cbranch_scc1 .Lsk_loop
	s_nop 3
	v_add_f32_dpp v108, v72, v73 quad_perm:[0,1,2,3] row_mask:0x1 bank_mask:0xf
	v_add_f32_dpp v108, v76, v77 quad_perm:[0,1,2,3] row_mask:0x2 bank_mask:0xf
	v_add_f32_dpp v108, v80, v81 quad_perm:[0,1,2,3] row_mask:0x4 bank_mask:0xf
	v_add_f32_dpp v108, v84, v85 quad_perm:[0,1,2,3] row_mask:0x8 bank_mask:0xf
	v_rcp_f32_e32 v109, v108
	s_mov_b32 s34, 0x3d0df4e0
	s_mov_b32 s35, s34
	v_mul_f32_e32 v118, v117, v109
	v_lshlrev_b32_e32 v72, 16, v0
	v_and_b32_e32 v73, 0xffff0000, v0
	v_log_f32_e32 v74, v72
	v_log_f32_e32 v75, v73
	s_nop 0
	v_pk_fma_f32 v[74:75], v[74:75], s[34:35], 1.0 op_sel_hi:[1,0,0]
	v_pk_mul_f32 v[74:75], v[74:75], v[72:73]
	v_cvt_pk_bf16_f32 v0, v74, v75
	v_lshlrev_b32_e32 v76, 16, v1
	v_and_b32_e32 v77, 0xffff0000, v1
	v_log_f32_e32 v78, v76
	v_log_f32_e32 v79, v77
	s_nop 0
	v_pk_fma_f32 v[78:79], v[78:79], s[34:35], 1.0 op_sel_hi:[1,0,0]
	v_pk_mul_f32 v[78:79], v[78:79], v[76:77]
	v_cvt_pk_bf16_f32 v1, v78, v79
	v_lshlrev_b32_e32 v80, 16, v2
	v_and_b32_e32 v81, 0xffff0000, v2
	v_log_f32_e32 v82, v80
	v_log_f32_e32 v83, v81
	s_nop 0
	v_pk_fma_f32 v[82:83], v[82:83], s[34:35], 1.0 op_sel_hi:[1,0,0]
	v_pk_mul_f32 v[82:83], v[82:83], v[80:81]
	v_cvt_pk_bf16_f32 v2, v82, v83
	v_lshlrev_b32_e32 v84, 16, v3
	v_and_b32_e32 v85, 0xffff0000, v3
	v_log_f32_e32 v86, v84
	v_log_f32_e32 v87, v85
	s_nop 0
	v_pk_fma_f32 v[86:87], v[86:87], s[34:35], 1.0 op_sel_hi:[1,0,0]
	v_pk_mul_f32 v[86:87], v[86:87], v[84:85]
	v_cvt_pk_bf16_f32 v3, v86, v87
	v_lshlrev_b32_e32 v72, 16, v4
	v_and_b32_e32 v73, 0xffff0000, v4
	v_log_f32_e32 v74, v72
	v_log_f32_e32 v75, v73
	s_nop 0
	v_pk_fma_f32 v[74:75], v[74:75], s[34:35], 1.0 op_sel_hi:[1,0,0]
	v_pk_mul_f32 v[74:75], v[74:75], v[72:73]
	v_cvt_pk_bf16_f32 v4, v74, v75
	v_lshlrev_b32_e32 v76, 16, v5
	v_and_b32_e32 v77, 0xffff0000, v5
	v_log_f32_e32 v78, v76
	v_log_f32_e32 v79, v77
	s_nop 0
	v_pk_fma_f32 v[78:79], v[78:79], s[34:35], 1.0 op_sel_hi:[1,0,0]
	v_pk_mul_f32 v[78:79], v[78:79], v[76:77]
	v_cvt_pk_bf16_f32 v5, v78, v79
	v_lshlrev_b32_e32 v80, 16, v6
	v_and_b32_e32 v81, 0xffff0000, v6
	v_log_f32_e32 v82, v80
	v_log_f32_e32 v83, v81
	s_nop 0
	v_pk_fma_f32 v[82:83], v[82:83], s[34:35], 1.0 op_sel_hi:[1,0,0]
	v_pk_mul_f32 v[82:83], v[82:83], v[80:81]
	v_cvt_pk_bf16_f32 v6, v82, v83
	v_lshlrev_b32_e32 v84, 16, v7
	v_and_b32_e32 v85, 0xffff0000, v7
	v_log_f32_e32 v86, v84
	v_log_f32_e32 v87, v85
	s_nop 0
	v_pk_fma_f32 v[86:87], v[86:87], s[34:35], 1.0 op_sel_hi:[1,0,0]
	v_pk_mul_f32 v[86:87], v[86:87], v[84:85]
	v_cvt_pk_bf16_f32 v7, v86, v87
	v_lshlrev_b32_e32 v72, 16, v8
	v_and_b32_e32 v73, 0xffff0000, v8
	v_log_f32_e32 v74, v72
	v_log_f32_e32 v75, v73
	s_nop 0
	v_pk_fma_f32 v[74:75], v[74:75], s[34:35], 1.0 op_sel_hi:[1,0,0]
	v_pk_mul_f32 v[74:75], v[74:75], v[72:73]
	v_cvt_pk_bf16_f32 v8, v74, v75
	v_lshlrev_b32_e32 v76, 16, v9
	v_and_b32_e32 v77, 0xffff0000, v9
	v_log_f32_e32 v78, v76
	v_log_f32_e32 v79, v77
	s_nop 0
	v_pk_fma_f32 v[78:79], v[78:79], s[34:35], 1.0 op_sel_hi:[1,0,0]
	v_pk_mul_f32 v[78:79], v[78:79], v[76:77]
	v_cvt_pk_bf16_f32 v9, v78, v79
	v_lshlrev_b32_e32 v80, 16, v10
	v_and_b32_e32 v81, 0xffff0000, v10
	v_log_f32_e32 v82, v80
	v_log_f32_e32 v83, v81
	s_nop 0
	v_pk_fma_f32 v[82:83], v[82:83], s[34:35], 1.0 op_sel_hi:[1,0,0]
	v_pk_mul_f32 v[82:83], v[82:83], v[80:81]
	v_cvt_pk_bf16_f32 v10, v82, v83
	v_lshlrev_b32_e32 v84, 16, v11
	v_and_b32_e32 v85, 0xffff0000, v11
	v_log_f32_e32 v86, v84
	v_log_f32_e32 v87, v85
	s_nop 0
	v_pk_fma_f32 v[86:87], v[86:87], s[34:35], 1.0 op_sel_hi:[1,0,0]
	v_pk_mul_f32 v[86:87], v[86:87], v[84:85]
	v_cvt_pk_bf16_f32 v11, v86, v87
	v_lshlrev_b32_e32 v72, 16, v12
	v_and_b32_e32 v73, 0xffff0000, v12
	v_log_f32_e32 v74, v72
	v_log_f32_e32 v75, v73
	s_nop 0
	v_pk_fma_f32 v[74:75], v[74:75], s[34:35], 1.0 op_sel_hi:[1,0,0]
	v_pk_mul_f32 v[74:75], v[74:75], v[72:73]
	v_cvt_pk_bf16_f32 v12, v74, v75
	v_lshlrev_b32_e32 v76, 16, v13
	v_and_b32_e32 v77, 0xffff0000, v13
	v_log_f32_e32 v78, v76
	v_log_f32_e32 v79, v77
	s_nop 0
	v_pk_fma_f32 v[78:79], v[78:79], s[34:35], 1.0 op_sel_hi:[1,0,0]
	v_pk_mul_f32 v[78:79], v[78:79], v[76:77]
	v_cvt_pk_bf16_f32 v13, v78, v79
	v_lshlrev_b32_e32 v80, 16, v14
	v_and_b32_e32 v81, 0xffff0000, v14
	v_log_f32_e32 v82, v80
	v_log_f32_e32 v83, v81
	s_nop 0
	v_pk_fma_f32 v[82:83], v[82:83], s[34:35], 1.0 op_sel_hi:[1,0,0]
	v_pk_mul_f32 v[82:83], v[82:83], v[80:81]
	v_cvt_pk_bf16_f32 v14, v82, v83
	v_lshlrev_b32_e32 v84, 16, v15
	v_and_b32_e32 v85, 0xffff0000, v15
	v_log_f32_e32 v86, v84
	v_log_f32_e32 v87, v85
	s_nop 0
	v_pk_fma_f32 v[86:87], v[86:87], s[34:35], 1.0 op_sel_hi:[1,0,0]
	v_pk_mul_f32 v[86:87], v[86:87], v[84:85]
	v_cvt_pk_bf16_f32 v15, v86, v87
	v_lshlrev_b32_e32 v72, 16, v16
	v_and_b32_e32 v73, 0xffff0000, v16
	v_log_f32_e32 v74, v72
	v_log_f32_e32 v75, v73
	s_nop 0
	v_pk_fma_f32 v[74:75], v[74:75], s[34:35], 1.0 op_sel_hi:[1,0,0]
	v_pk_mul_f32 v[74:75], v[74:75], v[72:73]
	v_cvt_pk_bf16_f32 v16, v74, v75
	v_lshlrev_b32_e32 v76, 16, v17
	v_and_b32_e32 v77, 0xffff0000, v17
	v_log_f32_e32 v78, v76
	v_log_f32_e32 v79, v77
	s_nop 0
	v_pk_fma_f32 v[78:79], v[78:79], s[34:35], 1.0 op_sel_hi:[1,0,0]
	v_pk_mul_f32 v[78:79], v[78:79], v[76:77]
	v_cvt_pk_bf16_f32 v17, v78, v79
	v_lshlrev_b32_e32 v80, 16, v18
	v_and_b32_e32 v81, 0xffff0000, v18
	v_log_f32_e32 v82, v80
	v_log_f32_e32 v83, v81
	s_nop 0
	v_pk_fma_f32 v[82:83], v[82:83], s[34:35], 1.0 op_sel_hi:[1,0,0]
	v_pk_mul_f32 v[82:83], v[82:83], v[80:81]
	v_cvt_pk_bf16_f32 v18, v82, v83
	v_lshlrev_b32_e32 v84, 16, v19
	v_and_b32_e32 v85, 0xffff0000, v19
	v_log_f32_e32 v86, v84
	v_log_f32_e32 v87, v85
	s_nop 0
	v_pk_fma_f32 v[86:87], v[86:87], s[34:35], 1.0 op_sel_hi:[1,0,0]
	v_pk_mul_f32 v[86:87], v[86:87], v[84:85]
	v_cvt_pk_bf16_f32 v19, v86, v87
	v_lshlrev_b32_e32 v72, 16, v20
	v_and_b32_e32 v73, 0xffff0000, v20
	v_log_f32_e32 v74, v72
	v_log_f32_e32 v75, v73
	s_nop 0
	v_pk_fma_f32 v[74:75], v[74:75], s[34:35], 1.0 op_sel_hi:[1,0,0]
	v_pk_mul_f32 v[74:75], v[74:75], v[72:73]
	v_cvt_pk_bf16_f32 v20, v74, v75
	v_lshlrev_b32_e32 v76, 16, v21
	v_and_b32_e32 v77, 0xffff0000, v21
	v_log_f32_e32 v78, v76
	v_log_f32_e32 v79, v77
	s_nop 0
	v_pk_fma_f32 v[78:79], v[78:79], s[34:35], 1.0 op_sel_hi:[1,0,0]
	v_pk_mul_f32 v[78:79], v[78:79], v[76:77]
	v_cvt_pk_bf16_f32 v21, v78, v79
	v_lshlrev_b32_e32 v80, 16, v22
	v_and_b32_e32 v81, 0xffff0000, v22
	v_log_f32_e32 v82, v80
	v_log_f32_e32 v83, v81
	s_nop 0
	v_pk_fma_f32 v[82:83], v[82:83], s[34:35], 1.0 op_sel_hi:[1,0,0]
	v_pk_mul_f32 v[82:83], v[82:83], v[80:81]
	v_cvt_pk_bf16_f32 v22, v82, v83
	v_lshlrev_b32_e32 v84, 16, v23
	v_and_b32_e32 v85, 0xffff0000, v23
	v_log_f32_e32 v86, v84
	v_log_f32_e32 v87, v85
	s_nop 0
	v_pk_fma_f32 v[86:87], v[86:87], s[34:35], 1.0 op_sel_hi:[1,0,0]
	v_pk_mul_f32 v[86:87], v[86:87], v[84:85]
	v_cvt_pk_bf16_f32 v23, v86, v87
	v_lshlrev_b32_e32 v72, 16, v24
	v_and_b32_e32 v73, 0xffff0000, v24
	v_log_f32_e32 v74, v72
	v_log_f32_e32 v75, v73
	s_nop 0
	v_pk_fma_f32 v[74:75], v[74:75], s[34:35], 1.0 op_sel_hi:[1,0,0]
	v_pk_mul_f32 v[74:75], v[74:75], v[72:73]
	v_cvt_pk_bf16_f32 v24, v74, v75
	v_lshlrev_b32_e32 v76, 16, v25
	v_and_b32_e32 v77, 0xffff0000, v25
	v_log_f32_e32 v78, v76
	v_log_f32_e32 v79, v77
	s_nop 0
	v_pk_fma_f32 v[78:79], v[78:79], s[34:35], 1.0 op_sel_hi:[1,0,0]
	v_pk_mul_f32 v[78:79], v[78:79], v[76:77]
	v_cvt_pk_bf16_f32 v25, v78, v79
	v_lshlrev_b32_e32 v80, 16, v26
	v_and_b32_e32 v81, 0xffff0000, v26
	v_log_f32_e32 v82, v80
	v_log_f32_e32 v83, v81
	s_nop 0
	v_pk_fma_f32 v[82:83], v[82:83], s[34:35], 1.0 op_sel_hi:[1,0,0]
	v_pk_mul_f32 v[82:83], v[82:83], v[80:81]
	v_cvt_pk_bf16_f32 v26, v82, v83
	v_lshlrev_b32_e32 v84, 16, v27
	v_and_b32_e32 v85, 0xffff0000, v27
	v_log_f32_e32 v86, v84
	v_log_f32_e32 v87, v85
	s_nop 0
	v_pk_fma_f32 v[86:87], v[86:87], s[34:35], 1.0 op_sel_hi:[1,0,0]
	v_pk_mul_f32 v[86:87], v[86:87], v[84:85]
	v_cvt_pk_bf16_f32 v27, v86, v87
	v_lshlrev_b32_e32 v72, 16, v28
	v_and_b32_e32 v73, 0xffff0000, v28
	v_log_f32_e32 v74, v72
	v_log_f32_e32 v75, v73
	s_nop 0
	v_pk_fma_f32 v[74:75], v[74:75], s[34:35], 1.0 op_sel_hi:[1,0,0]
	v_pk_mul_f32 v[74:75], v[74:75], v[72:73]
	v_cvt_pk_bf16_f32 v28, v74, v75
	v_lshlrev_b32_e32 v76, 16, v29
	v_and_b32_e32 v77, 0xffff0000, v29
	v_log_f32_e32 v78, v76
	v_log_f32_e32 v79, v77
	s_nop 0
	v_pk_fma_f32 v[78:79], v[78:79], s[34:35], 1.0 op_sel_hi:[1,0,0]
	v_pk_mul_f32 v[78:79], v[78:79], v[76:77]
	v_cvt_pk_bf16_f32 v29, v78, v79
	v_lshlrev_b32_e32 v80, 16, v30
	v_and_b32_e32 v81, 0xffff0000, v30
	v_log_f32_e32 v82, v80
	v_log_f32_e32 v83, v81
	s_nop 0
	v_pk_fma_f32 v[82:83], v[82:83], s[34:35], 1.0 op_sel_hi:[1,0,0]
	v_pk_mul_f32 v[82:83], v[82:83], v[80:81]
	v_cvt_pk_bf16_f32 v30, v82, v83
	v_lshlrev_b32_e32 v84, 16, v31
	v_and_b32_e32 v85, 0xffff0000, v31
	v_log_f32_e32 v86, v84
	v_log_f32_e32 v87, v85
	s_nop 0
	v_pk_fma_f32 v[86:87], v[86:87], s[34:35], 1.0 op_sel_hi:[1,0,0]
	v_pk_mul_f32 v[86:87], v[86:87], v[84:85]
	v_cvt_pk_bf16_f32 v31, v86, v87
	v_mov_b64_e32 v[88:89], s[32:33]
	v_mov_b64_e32 v[92:93], s[32:33]
	v_mov_b64_e32 v[96:97], s[32:33]
	v_mov_b64_e32 v[104:105], s[32:33]
	s_nop 1
	v_smfmac_f32_16x16x64_bf16 v[88:91], v[68:71], v[0:7], v64
	v_smfmac_f32_16x16x64_bf16 v[92:95], v[68:71], v[8:15], v64
	v_smfmac_f32_16x16x64_bf16 v[96:99], v[68:71], v[16:23], v64
	v_smfmac_f32_16x16x64_bf16 v[104:107], v[68:71], v[24:31], v64
	s_nop 4
	v_add_f32_dpp v108, v88, v89 quad_perm:[0,1,2,3] row_mask:0x1 bank_mask:0xf
	v_add_f32_dpp v108, v92, v93 quad_perm:[0,1,2,3] row_mask:0x2 bank_mask:0xf
	v_add_f32_dpp v108, v96, v97 quad_perm:[0,1,2,3] row_mask:0x4 bank_mask:0xf
	v_add_f32_dpp v108, v104, v105 quad_perm:[0,1,2,3] row_mask:0x8 bank_mask:0xf
	v_add_f32_e32 v108, 0xab8cbccc, v108
	v_mul_f32_e32 v108, v118, v108
	s_nop 1
	v_add_f32_dpp v108, v108, v108 row_ror:8 row_mask:0xf bank_mask:0xf
	s_nop 1
	v_add_f32_dpp v108, v108, v108 row_ror:4 row_mask:0xf bank_mask:0xf
	s_nop 1
	v_add_f32_dpp v108, v108, v108 row_ror:2 row_mask:0xf bank_mask:0xf
	s_nop 1
	v_add_f32_dpp v108, v108, v108 row_ror:1 row_mask:0xf bank_mask:0xf
	s_nop 1
	v_mov_b32_e32 v109, v108
	s_nop 1
	v_permlane16_swap_b32_e32 v108, v109
	v_add_f32_e32 v108, v108, v109
	v_mov_b32_e32 v109, v108
	s_nop 1
	v_permlane32_swap_b32_e32 v108, v109
	v_add_f32_e32 v108, v108, v109
	v_cmp_eq_u32_e32 vcc, 0, v100
	s_and_saveexec_b64 s[0:1], vcc
	s_cbranch_execz .LBB1_38
	s_mul_i32 s0, s22, 5
	s_add_i32 s0, s0, s23
	s_mov_b32 s1, 0
	s_lshl_b64 s[0:1], s[0:1], 2
	s_add_u32 s0, s12, s0
	s_addc_u32 s1, s13, s1
	v_mov_b32_e32 v109, 0
	global_store_dword v109, v108, s[0:1]
